# P1: next unit's first-trip A half-tile pairs issued before the epilogue (ahead of its 16 stores in the VMEM queue); first-trip waits W1-W3 of later units 24/22/24 so the store drain overlaps the trip
# baseline (speedup 1.0000x reference)
; #define PG8_STAGE(bufoff, gbase, voff) do { PG8_GLDS((const char*)(gbase), (voff)[0], ldsb + (bufoff)); PG8_GLDS((const char*)(gbase), (voff)[1], ldsb + (bufoff) + 8192u); } while (0)
; #define PG8_STAGEA(bufoff, gbase, o0, o1) do { PG8_GLDS((const char*)(gbase), (o0), ldsb + (bufoff)); PG8_GLDS((const char*)(gbase), (o1), ldsb + (bufoff) + 8192u); } while (0)
; #define PG8_STAGEA1(bufoff, gbase) do { if constexpr (Sched::GATHER) { PG8_STAGEA(bufoff, gbase, vA2, vA3); } else { PG8_STAGEA(bufoff, (gbase) + hstep, vA0, vA1); } } while (0)
; #define PG8_WAIT_V(n) asm volatile("s_waitcnt vmcnt(" #n ")" ::: "memory")
; #define PG8_BAR __builtin_amdgcn_s_barrier()
; template <class Epi, class Sched, bool F8 = false, bool PF = false, bool I8 = false, int PID = -1>
; __device__ __forceinline__ void gemm_phase(LAS unsigned char* lds, LAS unsigned char* xlds, const int RP, const int RPB, const int nt, const Sched& S, const Epi& E, const int stagger_ticks) {
;     ...
;     PG8_ZERO_ACC();
;     PG8_STAGE(PG8_SB(0, 0), cB, voffB); PG8_STAGE(PG8_SB(0, 1), cB + hstepB, voffB); PG8_STAGEA(PG8_SA(0, 0), cA, vA0, vA1); PG8_STAGEA1(PG8_SA(0, 1), cA);
;     if (wr == 1) PG8_BAR;
;     PG8_WAIT_V(2); PG8_BAR;
;     PG8_STAGE(PG8_SB(1, 0), cB + kstep, voffB); PG8_STAGEA(PG8_SA(1, 0), cA + kstep, vA0, vA1); PG8_STAGE(PG8_SB(1, 1), cB + hstepB + kstep, voffB);
;     PG8_WAIT_V(6); PG8_BAR;
.LBB0_209:
	v_cndmask_b32_e64 v48, 0, 1, s[42:43]
	s_movk_i32 s23, 0x3c0
	v_readfirstlane_b32 s65, v48
	v_and_b32_e32 v48, 48, v46
	v_lshlrev_b32_e32 v46, 6, v46
	s_and_b32 s19, s46, 3
	s_lshl_b32 s64, s8, 6
	s_lshl_b32 s8, s8, 13
	v_and_or_b32 v46, v46, s23, v48
	v_and_b32_e32 v47, 32, v47
	v_bitop3_b32 v48, v46, s8, v47 bitop3:0xde
	s_lshl_b32 s8, s19, 12
	s_add_u32 s42, s12, 0x80
	v_bitop3_b32 v46, v46, s8, v47 bitop3:0xde
	s_addc_u32 s43, s13, 0
	s_add_i32 s8, s7, 0x18000
	s_waitcnt vmcnt(2)
	s_barrier
	s_mov_b32 m0, s8
	s_nop 0
	global_load_lds_dwordx4 v182, s[42:43]
	s_add_i32 s8, s7, 0x1a000
	s_mov_b32 m0, s8
	s_nop 0
	global_load_lds_dwordx4 v183, s[42:43]
	s_add_u32 s42, s10, 0x80
	s_addc_u32 s43, s11, 0
	s_add_i32 s8, s7, 0x8000
	s_mov_b32 m0, s8
	s_nop 0
	global_load_lds_dwordx4 v180, s[42:43]
	s_add_i32 s8, s7, 0xa000
	s_mov_b32 m0, s8
	s_nop 0
	global_load_lds_dwordx4 v181, s[42:43]
	s_add_u32 s42, s12, 0x2080
	s_addc_u32 s43, s13, 0
	s_add_i32 s8, s7, 0x1c000
	s_mov_b32 m0, s8
	s_nop 0
	global_load_lds_dwordx4 v182, s[42:43]
	s_add_i32 s8, s7, 0x1e000
	s_mov_b32 m0, s8
	s_nop 0
	global_load_lds_dwordx4 v183, s[42:43]
	s_waitcnt vmcnt(6)
	s_cmpk_lt_u32 s44, 0x100
	s_cselect_b64 s[42:43], -1, 0
	s_lshl_b32 s66, s19, 6
	s_mov_b32 s67, 0x4704000
	s_mov_b32 s69, 0x4680000
	s_mov_b32 s8, 0x3d372713
	s_mov_b32 s44, 0xc0135761
	s_mov_b32 s70, 0x25000000
	s_movk_i32 s71, 0xa00
	s_mov_b32 s72, 0x1d000000
	s_mov_b32 s73, 0xa00000
	v_add_u32_e32 v184, 0, v46
	v_add_u32_e32 v185, 0, v48
	s_barrier
	s_mov_b32 s99, 0
	s_branch .LBB0_212

; #define PG8_UNI64(p) ((const char*)((((unsigned long long)(unsigned)__builtin_amdgcn_readfirstlane((int)((unsigned long long)(p) >> 32))) << 32) | (unsigned long long)(unsigned)__builtin_amdgcn_readfirstlane((int)(unsigned)(unsigned long long)(p))))
; #define PG8_BAR __builtin_amdgcn_s_barrier()
; #define PROF_BEGIN(sel) do { if constexpr (PROF && PROF_SEL == (sel)) prof_t0 = (unsigned)__builtin_amdgcn_s_memrealtime(); } while (0)
;     __device__ __forceinline__ const char* Abase(const pg8::Unit& u) const { size_t o = WS_R1; if (u.aux == 1) o = WS_R3; return ws + o + (size_t)u.pm * TSF8; }
;     __device__ __forceinline__ const char* Bbase(const pg8::Unit& u) const { size_t o = WS_WIN; if (u.aux == 1) o = WS_WKV; return ws + o + (size_t)u.pn * TSF8; }
;     __device__ __forceinline__ const char* Abase(const pg8::Unit& u) const { if (GATH) return ws + WS_XQ; return ws + WS_H2 + (size_t)u.pm * TSF8; }
; template <class Epi, class Sched, bool F8 = false, bool PF = false, bool I8 = false, int PID = -1>
; __device__ __forceinline__ void gemm_phase(LAS unsigned char* lds, LAS unsigned char* xlds, const int RP, const int RPB, const int nt, const Sched& S, const Epi& E, const int stagger_ticks) {
;     ...
;         if (!has_next) break;
;         PROF_BEGIN(3);
;         cur = nxt; cA = nA; cB = nB; ++ui;
;         has_next = has_nn; nxt = nn;
;         if (has_next) { nA = PG8_UNI64(S.Abase(nxt)); nB = PG8_UNI64(S.Bbase(nxt)); }
;         if (Sched::GATHER) { *nslot = (u32x4){gv[0], gv[1], gv[2], gv[3]}; asm volatile("" ::: "memory"); }
;         PG8_ZERO_ACC();
;         if (wr == 1) PG8_BAR;
.LBB0_211:
	s_and_b64 vcc, exec, s[46:47]
	s_cbranch_vccnz .LBB0_263
	s_mov_b32 s99, 1

; #define PG8_STAGEA1(bufoff, gbase) do { if constexpr (Sched::GATHER) { PG8_STAGEA(bufoff, gbase, vA2, vA3); } else { PG8_STAGEA(bufoff, (gbase) + hstep, vA0, vA1); } } while (0)
; #define PG8_LDA(dst, b, h) do { if constexpr (F8) { _Pragma("unroll") for (int m = 0; m < 4; ++m) dst##8[m] = PG8_LD32(lds + PG8_SA(b, h) + aoff + m * 2048); } else { \
;         _Pragma("unroll") for (int m = 0; m < 4; ++m) _Pragma("unroll") for (int k = 0; k < 2; ++k) dst[m][k] = *(const LAS bf16x8*)(lds + PG8_SA(b, h) + aoff + m * 2048 + k * 1024); } } while (0)
; #define PG8_WAIT_VX() do { if (relax) asm volatile("s_waitcnt vmcnt(%0)" :: "n"(8 + Epi::RELAX) : "memory"); else PG8_WAIT_V(8); } while (0)
; #define PG8_WAIT_L(n) asm volatile("s_waitcnt lgkmcnt(" #n ")" ::: "memory")
; #define PG8_BAR __builtin_amdgcn_s_barrier()
; template <class Epi, class Sched, bool F8 = false, bool PF = false, bool I8 = false, int PID = -1>
; __device__ __forceinline__ void gemm_phase(LAS unsigned char* lds, LAS unsigned char* xlds, const int RP, const int RPB, const int nt, const Sched& S, const Epi& E, const int stagger_ticks) {
;     ...
;         for (int t = 0; t < nt; t += 2) {
;             const bool last = (t == nt - 2);
;             unsigned ldsb = ldsb0; asm volatile("" : "+s"(ldsb));
;             const char* a1 = cA + (size_t)(t + 1) * kstep;
;             const char* a2 = last ? nA : cA + (size_t)(t + 2) * kstep; const char* b2 = last ? nB : cB + (size_t)(t + 2) * kstep;
;             const char* a3 = a2 + kstep; const char* b3 = b2 + kstep;
;             if constexpr (PF) { const char* pfa = (t + 4 < nt) ? cA + (size_t)(t + 4) * kstep : nA + (size_t)(t + 4 - nt) * kstep;
;                 asm volatile("s_mov_b32 m0, %2\n\ts_nop 0\n\tglobal_load_lds_dword %0, %1" :: "v"(voffP), "s"(pfa), "s"(ldsP) : "memory", "m0"); }
;             const bool relax = (Epi::RELAX > 0) && (t == 0) && epi_ran;
;             PG8_LDB(B0, 0, 0); PG8_LDB(B1, 0, 1); PG8_SCHED; PG8_LDA(At, 0, 0); PG8_STAGEA1(PG8_SA(1, 1), a1);
;             if (Sched::GATHER) { if (last) { const u32x4 nv = *nslot; vA0 = nv.x; vA1 = nv.y; vA2 = nv.z; vA3 = nv.w; } }
;             PG8_WAIT_VX(); PG8_WAIT_L(0); PG8_BAR; PG8_MMA(0, 0, At, B0); PG8_MMA(0, 1, At, B1); PG8_BAR; PG8_SCHED;
;             if constexpr (Epi::BIAS_DMA) { if (t == 0 && has_next) E.bias_dma(nxt, xlds + 8192 + ((ui + 1) & 1) * Epi::BIAS_STRIDE, wid, lane); }
.Lmy_z1t:
	s_mov_b32 s82, s7
	s_cmp_lg_u32 s99, 0
	s_cbranch_scc1 .Lmy_h1a
	s_add_u32 s100, s2, 0xfffe0000
	s_addc_u32 s101, s3, -1
	s_add_i32 s48, s82, 0x8000
	s_mov_b32 m0, s48
	s_nop 0
	global_load_lds_dwordx4 v180, s[100:101]
	s_add_i32 s48, s82, 0xa000
	s_mov_b32 m0, s48
	s_nop 0
	global_load_lds_dwordx4 v181, s[100:101]
.Lmy_h1a:
	v_add_u32_e32 v46, 0x10000, v184
	ds_read_b128 v[162:165], v46
	ds_read_b128 v[166:169], v46 offset:1024
	ds_read_b128 v[170:173], v46 offset:2048
	ds_read_b128 v[174:177], v46 offset:3072
	v_add_u32_e32 v46, 0x14000, v184
	ds_read_b128 v[146:149], v46
	ds_read_b128 v[150:153], v46 offset:1024
	ds_read_b128 v[154:157], v46 offset:2048
	ds_read_b128 v[158:161], v46 offset:3072
	ds_read_b128 v[186:189], v185
	ds_read_b128 v[190:193], v185 offset:1024
	ds_read_b128 v[194:197], v185 offset:2048
	ds_read_b128 v[198:201], v185 offset:3072
	ds_read_b128 v[202:205], v185 offset:4096
	ds_read_b128 v[206:209], v185 offset:5120
	ds_read_b128 v[210:213], v185 offset:6144
	ds_read_b128 v[214:217], v185 offset:7168
	s_cmp_lg_u32 s99, 0
	s_cbranch_scc1 .Lmy_h1b
	s_add_i32 s48, s82, 0xc000
	s_mov_b32 m0, s48
	s_nop 0
	global_load_lds_dwordx4 v180, s[2:3]
	s_add_i32 s48, s82, 0xe000
	s_mov_b32 m0, s48
	s_nop 0
	global_load_lds_dwordx4 v181, s[2:3]
.Lmy_h1b:
	s_cmp_lg_u32 s99, 0
	s_cbranch_scc1 .Lmy_rw0a
	s_waitcnt vmcnt(8)
	s_branch .Lmy_rw0b
.Lmy_rw0a:
	s_waitcnt vmcnt(24)
.Lmy_rw0b:
	s_waitcnt lgkmcnt(0)
	s_barrier
	s_setprio 1
	s_waitcnt lgkmcnt(7)
	v_mfma_i32_16x16x64_i8 v[46:49], v[162:165], v[186:189], 0
	v_mfma_i32_16x16x64_i8 v[54:57], v[170:173], v[186:189], 0
	s_waitcnt lgkmcnt(5)
	v_mfma_i32_16x16x64_i8 v[58:61], v[162:165], v[194:197], 0
	v_mfma_i32_16x16x64_i8 v[66:69], v[170:173], v[194:197], 0
	s_waitcnt lgkmcnt(3)
	v_mfma_i32_16x16x64_i8 v[110:113], v[162:165], v[202:205], 0
	v_mfma_i32_16x16x64_i8 v[106:109], v[170:173], v[202:205], 0
	s_waitcnt lgkmcnt(1)
	v_mfma_i32_16x16x64_i8 v[94:97], v[162:165], v[210:213], 0
	v_mfma_i32_16x16x64_i8 v[90:93], v[170:173], v[210:213], 0
	v_mfma_i32_16x16x64_i8 v[46:49], v[166:169], v[190:193], v[46:49]
	v_mfma_i32_16x16x64_i8 v[54:57], v[174:177], v[190:193], v[54:57]
	v_mfma_i32_16x16x64_i8 v[58:61], v[166:169], v[198:201], v[58:61]
	v_mfma_i32_16x16x64_i8 v[66:69], v[174:177], v[198:201], v[66:69]
	v_mfma_i32_16x16x64_i8 v[110:113], v[166:169], v[206:209], v[110:113]
	v_mfma_i32_16x16x64_i8 v[106:109], v[174:177], v[206:209], v[106:109]
	s_waitcnt lgkmcnt(0)
	v_mfma_i32_16x16x64_i8 v[94:97], v[166:169], v[214:217], v[94:97]
	v_mfma_i32_16x16x64_i8 v[90:93], v[174:177], v[214:217], v[90:93]
	v_mfma_i32_16x16x64_i8 v[122:125], v[146:149], v[186:189], 0
	v_mfma_i32_16x16x64_i8 v[134:137], v[150:153], v[190:193], v[122:125]
	v_mfma_i32_16x16x64_i8 v[122:125], v[154:157], v[186:189], 0
	v_mfma_i32_16x16x64_i8 v[118:121], v[146:149], v[194:197], 0
	v_mfma_i32_16x16x64_i8 v[114:117], v[154:157], v[194:197], 0
	v_mfma_i32_16x16x64_i8 v[102:105], v[146:149], v[202:205], 0
	v_mfma_i32_16x16x64_i8 v[98:101], v[154:157], v[202:205], 0
	v_mfma_i32_16x16x64_i8 v[86:89], v[146:149], v[210:213], 0
	v_mfma_i32_16x16x64_i8 v[82:85], v[154:157], v[210:213], 0
	v_mfma_i32_16x16x64_i8 v[130:133], v[158:161], v[190:193], v[122:125]
	v_mfma_i32_16x16x64_i8 v[118:121], v[150:153], v[198:201], v[118:121]
	v_mfma_i32_16x16x64_i8 v[114:117], v[158:161], v[198:201], v[114:117]
	v_mfma_i32_16x16x64_i8 v[102:105], v[150:153], v[206:209], v[102:105]
	v_mfma_i32_16x16x64_i8 v[98:101], v[158:161], v[206:209], v[98:101]
	v_mfma_i32_16x16x64_i8 v[86:89], v[150:153], v[214:217], v[86:89]
	v_mfma_i32_16x16x64_i8 v[82:85], v[158:161], v[214:217], v[82:85]
	s_setprio 0
	s_barrier
	s_cmp_lg_u32 s79, -2
	s_cselect_b64 s[48:49], -1, 0
	s_or_b64 s[48:49], s[46:47], s[48:49]
	s_and_b64 vcc, exec, s[48:49]
	s_cbranch_vccnz .Lmy_z1b
	s_mov_b32 m0, s78
	s_nop 0
	global_load_lds_dword v1, s[0:1]
	s_branch .Lmy_z1b
; #define PG8_STAGE(bufoff, gbase, voff) do { PG8_GLDS((const char*)(gbase), (voff)[0], ldsb + (bufoff)); PG8_GLDS((const char*)(gbase), (voff)[1], ldsb + (bufoff) + 8192u); } while (0)
; #define PG8_STAGEA(bufoff, gbase, o0, o1) do { PG8_GLDS((const char*)(gbase), (o0), ldsb + (bufoff)); PG8_GLDS((const char*)(gbase), (o1), ldsb + (bufoff) + 8192u); } while (0)
; #define PG8_STAGEA1(bufoff, gbase) do { if constexpr (Sched::GATHER) { PG8_STAGEA(bufoff, gbase, vA2, vA3); } else { PG8_STAGEA(bufoff, (gbase) + hstep, vA0, vA1); } } while (0)
; #define PG8_LDA(dst, b, h) do { if constexpr (F8) { _Pragma("unroll") for (int m = 0; m < 4; ++m) dst##8[m] = PG8_LD32(lds + PG8_SA(b, h) + aoff + m * 2048); } else { \
;         _Pragma("unroll") for (int m = 0; m < 4; ++m) _Pragma("unroll") for (int k = 0; k < 2; ++k) dst[m][k] = *(const LAS bf16x8*)(lds + PG8_SA(b, h) + aoff + m * 2048 + k * 1024); } } while (0)
; #define PG8_LDB(dst, b, h) do { if constexpr (F8) { _Pragma("unroll") for (int n = 0; n < 2; ++n) dst##8[n] = PG8_LD32(lds + PG8_SB(b, h) + boff + n * 2048); } else { \
;         _Pragma("unroll") for (int n = 0; n < 2; ++n) _Pragma("unroll") for (int k = 0; k < 2; ++k) dst[n][k] = *(const LAS bf16x8*)(lds + PG8_SB(b, h) + boff + n * 2048 + k * 1024); } } while (0)
; #define PG8_WAIT_VR() PG8_WAIT_V(8)
; #define PG8_WAIT_VX() do { if (relax) asm volatile("s_waitcnt vmcnt(%0)" :: "n"(8 + Epi::RELAX) : "memory"); else PG8_WAIT_V(8); } while (0)
; #define PG8_WAIT_L(n) asm volatile("s_waitcnt lgkmcnt(" #n ")" ::: "memory")
; #define PG8_BAR __builtin_amdgcn_s_barrier()
; template <class Epi, class Sched, bool F8 = false, bool PF = false, bool I8 = false, int PID = -1>
; __device__ __forceinline__ void gemm_phase(LAS unsigned char* lds, LAS unsigned char* xlds, const int RP, const int RPB, const int nt, const Sched& S, const Epi& E, const int stagger_ticks) {
;     ...
;             PG8_LDA(At, 0, 1); PG8_STAGE(PG8_SB(0, 0), b2, voffB); PG8_STAGE(PG8_SB(0, 1), b2 + hstepB, voffB); PG8_STAGEA(PG8_SA(0, 0), a2, vA0, vA1);
;             PG8_WAIT_VX(); PG8_WAIT_L(0); PG8_BAR; PG8_MMA(1, 0, At, B0); PG8_MMA(1, 1, At, B1); PG8_BAR; PG8_SCHED;
;             PG8_LDB(B0, 1, 0); PG8_LDB(B1, 1, 1); PG8_SCHED; PG8_LDA(At, 1, 0); PG8_STAGEA1(PG8_SA(0, 1), a2);
;             PG8_WAIT_VR(); PG8_WAIT_L(0); PG8_BAR; PG8_MMA(0, 0, At, B0); PG8_MMA(0, 1, At, B1); PG8_BAR; PG8_SCHED;
.Lmy_z1b:
	s_add_u32 s48, s2, 0xfffe0080
	s_addc_u32 s49, s3, -1
	s_cmp_eq_u32 s79, 4
	s_cselect_b32 s62, s10, s48
	s_cselect_b32 s63, s11, s49
	s_cselect_b32 s50, s12, s76
	s_cselect_b32 s51, s13, s77
	s_add_u32 s48, s62, 0x80
	s_addc_u32 s49, s63, 0
	s_add_u32 s60, s50, 0x80
	s_addc_u32 s61, s51, 0
	ds_read_b128 v[122:125], v185 offset:16384
	ds_read_b128 v[126:129], v185 offset:17408
	ds_read_b128 v[138:141], v185 offset:18432
	ds_read_b128 v[142:145], v185 offset:19456
	ds_read_b128 v[186:189], v185 offset:20480
	ds_read_b128 v[190:193], v185 offset:21504
	ds_read_b128 v[194:197], v185 offset:22528
	ds_read_b128 v[198:201], v185 offset:23552
	s_add_i32 s83, s82, 0x10000
	s_mov_b32 m0, s83
	s_nop 0
	global_load_lds_dwordx4 v182, s[50:51]
	s_add_i32 s83, s82, 0x12000
	s_mov_b32 m0, s83
	s_nop 0
	global_load_lds_dwordx4 v183, s[50:51]
	s_add_u32 s86, s50, 0x2000
	s_addc_u32 s87, s51, 0
	s_add_i32 s83, s82, 0x14000
	s_mov_b32 m0, s83
	s_nop 0
	global_load_lds_dwordx4 v182, s[86:87]
	s_add_i32 s83, s82, 0x16000
	s_mov_b32 m0, s83
	s_nop 0
	global_load_lds_dwordx4 v183, s[86:87]
	s_cmp_lg_u32 s99, 0
	s_cbranch_scc1 .Lmy_rw1a
	s_waitcnt vmcnt(6)
	s_branch .Lmy_rw1b
.Lmy_rw1a:
	s_waitcnt vmcnt(22)
.Lmy_rw1b:
	s_waitcnt lgkmcnt(0)
	s_barrier
	s_setprio 1
	s_waitcnt lgkmcnt(7)
	v_mfma_i32_16x16x64_i8 v[78:81], v[162:165], v[122:125], 0
	v_mfma_i32_16x16x64_i8 v[74:77], v[170:173], v[122:125], 0
	s_waitcnt lgkmcnt(5)
	v_mfma_i32_16x16x64_i8 v[50:53], v[162:165], v[138:141], 0
	v_mfma_i32_16x16x64_i8 v[42:45], v[170:173], v[138:141], 0
	s_waitcnt lgkmcnt(3)
	v_mfma_i32_16x16x64_i8 v[30:33], v[162:165], v[186:189], 0
	v_mfma_i32_16x16x64_i8 v[26:29], v[170:173], v[186:189], 0
	s_waitcnt lgkmcnt(1)
	v_mfma_i32_16x16x64_i8 v[14:17], v[162:165], v[194:197], 0
	v_mfma_i32_16x16x64_i8 v[10:13], v[170:173], v[194:197], 0
	v_mfma_i32_16x16x64_i8 v[78:81], v[166:169], v[126:129], v[78:81]
	v_mfma_i32_16x16x64_i8 v[74:77], v[174:177], v[126:129], v[74:77]
	v_mfma_i32_16x16x64_i8 v[50:53], v[166:169], v[142:145], v[50:53]
	v_mfma_i32_16x16x64_i8 v[42:45], v[174:177], v[142:145], v[42:45]
	v_mfma_i32_16x16x64_i8 v[30:33], v[166:169], v[190:193], v[30:33]
	v_mfma_i32_16x16x64_i8 v[26:29], v[174:177], v[190:193], v[26:29]
	s_waitcnt lgkmcnt(0)
	v_mfma_i32_16x16x64_i8 v[14:17], v[166:169], v[198:201], v[14:17]
	v_mfma_i32_16x16x64_i8 v[10:13], v[174:177], v[198:201], v[10:13]
	v_mfma_i32_16x16x64_i8 v[70:73], v[146:149], v[122:125], 0
	v_mfma_i32_16x16x64_i8 v[62:65], v[154:157], v[122:125], 0
	v_mfma_i32_16x16x64_i8 v[38:41], v[146:149], v[138:141], 0
	v_mfma_i32_16x16x64_i8 v[34:37], v[154:157], v[138:141], 0
	v_mfma_i32_16x16x64_i8 v[22:25], v[146:149], v[186:189], 0
	v_mfma_i32_16x16x64_i8 v[18:21], v[154:157], v[186:189], 0
	v_mfma_i32_16x16x64_i8 v[6:9], v[146:149], v[194:197], 0
	v_mfma_i32_16x16x64_i8 v[2:5], v[154:157], v[194:197], 0
	v_mfma_i32_16x16x64_i8 v[70:73], v[150:153], v[126:129], v[70:73]
	v_mfma_i32_16x16x64_i8 v[62:65], v[158:161], v[126:129], v[62:65]
	v_mfma_i32_16x16x64_i8 v[38:41], v[150:153], v[142:145], v[38:41]
	v_mfma_i32_16x16x64_i8 v[34:37], v[158:161], v[142:145], v[34:37]
	v_mfma_i32_16x16x64_i8 v[22:25], v[150:153], v[190:193], v[22:25]
	v_mfma_i32_16x16x64_i8 v[18:21], v[158:161], v[190:193], v[18:21]
	v_mfma_i32_16x16x64_i8 v[6:9], v[150:153], v[198:201], v[6:9]
	v_mfma_i32_16x16x64_i8 v[2:5], v[158:161], v[198:201], v[2:5]
	s_setprio 0
	s_barrier
	s_add_i32 s83, s82, 0x2000
	s_mov_b32 m0, s82
	s_nop 0
	global_load_lds_dwordx4 v180, s[62:63]
	s_nop 0
	s_mov_b32 m0, s83
	s_nop 0
	global_load_lds_dwordx4 v181, s[62:63]
	v_add_u32_e32 v122, 0x18000, v184
	ds_read_b128 v[146:149], v122
	ds_read_b128 v[150:153], v122 offset:1024
	ds_read_b128 v[154:157], v122 offset:2048
	ds_read_b128 v[158:161], v122 offset:3072
	v_add_u32_e32 v122, 0x1c000, v184
	ds_read_b128 v[162:165], v122
	ds_read_b128 v[166:169], v122 offset:1024
	ds_read_b128 v[170:173], v122 offset:2048
	ds_read_b128 v[174:177], v122 offset:3072
	ds_read_b128 v[186:189], v185 offset:32768
	ds_read_b128 v[190:193], v185 offset:33792
	ds_read_b128 v[194:197], v185 offset:34816
	ds_read_b128 v[198:201], v185 offset:35840
	ds_read_b128 v[202:205], v185 offset:36864
	ds_read_b128 v[206:209], v185 offset:37888
	ds_read_b128 v[210:213], v185 offset:38912
	ds_read_b128 v[214:217], v185 offset:39936
	s_add_u32 s62, s62, 0x20000
	s_addc_u32 s63, s63, 0
	s_add_i32 s83, s82, 0x4000
	s_mov_b32 m0, s83
	s_nop 0
	global_load_lds_dwordx4 v180, s[62:63]
	s_add_i32 s83, s82, 0x6000
	s_mov_b32 m0, s83
	s_nop 0
	global_load_lds_dwordx4 v181, s[62:63]
	s_cmp_lg_u32 s99, 0
	s_cbranch_scc1 .Lmy_rw2a
	s_waitcnt vmcnt(8)
	s_branch .Lmy_rw2b

; #define PG8_STAGE(bufoff, gbase, voff) do { PG8_GLDS((const char*)(gbase), (voff)[0], ldsb + (bufoff)); PG8_GLDS((const char*)(gbase), (voff)[1], ldsb + (bufoff) + 8192u); } while (0)
; #define PG8_STAGEA(bufoff, gbase, o0, o1) do { PG8_GLDS((const char*)(gbase), (o0), ldsb + (bufoff)); PG8_GLDS((const char*)(gbase), (o1), ldsb + (bufoff) + 8192u); } while (0)
; #define PG8_LDA(dst, b, h) do { if constexpr (F8) { _Pragma("unroll") for (int m = 0; m < 4; ++m) dst##8[m] = PG8_LD32(lds + PG8_SA(b, h) + aoff + m * 2048); } else { \
;         _Pragma("unroll") for (int m = 0; m < 4; ++m) _Pragma("unroll") for (int k = 0; k < 2; ++k) dst[m][k] = *(const LAS bf16x8*)(lds + PG8_SA(b, h) + aoff + m * 2048 + k * 1024); } } while (0)
; #define PG8_WAIT_VR() PG8_WAIT_V(8)
; #define PG8_WAIT_L(n) asm volatile("s_waitcnt lgkmcnt(" #n ")" ::: "memory")
; #define PG8_BAR __builtin_amdgcn_s_barrier()
; #define PG8_SCHED __builtin_amdgcn_sched_barrier(0)
; template <class Epi, class Sched, bool F8 = false, bool PF = false, bool I8 = false, int PID = -1>
; __device__ __forceinline__ void gemm_phase(LAS unsigned char* lds, LAS unsigned char* xlds, const int RP, const int RPB, const int nt, const Sched& S, const Epi& E, const int stagger_ticks) {
;     ...
;             PG8_WAIT_VR(); PG8_WAIT_L(0); PG8_BAR; PG8_MMA(0, 0, At, B0); PG8_MMA(0, 1, At, B1); PG8_BAR; PG8_SCHED;
;             PG8_LDA(At, 1, 1); PG8_STAGE(PG8_SB(1, 0), b3, voffB); PG8_STAGE(PG8_SB(1, 1), b3 + hstepB, voffB); PG8_STAGEA(PG8_SA(1, 0), a3, vA0, vA1);
;             PG8_WAIT_VR(); PG8_WAIT_L(0); PG8_BAR; PG8_MMA(1, 0, At, B0); PG8_MMA(1, 1, At, B1); PG8_BAR; PG8_SCHED;
;         }
.Lmy_rw2b:
	s_waitcnt lgkmcnt(0)
	s_barrier
	s_setprio 1
	s_waitcnt lgkmcnt(7)
	v_mfma_i32_16x16x64_i8 v[46:49], v[146:149], v[186:189], v[46:49]
	s_waitcnt lgkmcnt(6)
	v_mfma_i32_16x16x64_i8 v[142:145], v[150:153], v[190:193], v[46:49]
	v_mfma_i32_16x16x64_i8 v[46:49], v[154:157], v[186:189], v[54:57]
	v_mfma_i32_16x16x64_i8 v[138:141], v[158:161], v[190:193], v[46:49]
	s_waitcnt lgkmcnt(5)
	v_mfma_i32_16x16x64_i8 v[46:49], v[146:149], v[194:197], v[58:61]
	s_waitcnt lgkmcnt(4)
	v_mfma_i32_16x16x64_i8 v[126:129], v[150:153], v[198:201], v[46:49]
	v_mfma_i32_16x16x64_i8 v[46:49], v[154:157], v[194:197], v[66:69]
	v_mfma_i32_16x16x64_i8 v[122:125], v[158:161], v[198:201], v[46:49]
	s_waitcnt lgkmcnt(3)
	v_mfma_i32_16x16x64_i8 v[46:49], v[146:149], v[202:205], v[110:113]
	s_waitcnt lgkmcnt(2)
	v_mfma_i32_16x16x64_i8 v[110:113], v[150:153], v[206:209], v[46:49]
	v_mfma_i32_16x16x64_i8 v[46:49], v[154:157], v[202:205], v[106:109]
	v_mfma_i32_16x16x64_i8 v[106:109], v[158:161], v[206:209], v[46:49]
	s_waitcnt lgkmcnt(1)
	v_mfma_i32_16x16x64_i8 v[46:49], v[146:149], v[210:213], v[94:97]
	s_waitcnt lgkmcnt(0)
	v_mfma_i32_16x16x64_i8 v[94:97], v[150:153], v[214:217], v[46:49]
	v_mfma_i32_16x16x64_i8 v[46:49], v[154:157], v[210:213], v[90:93]
	v_mfma_i32_16x16x64_i8 v[90:93], v[158:161], v[214:217], v[46:49]
	v_mfma_i32_16x16x64_i8 v[46:49], v[162:165], v[186:189], v[134:137]
	v_mfma_i32_16x16x64_i8 v[134:137], v[166:169], v[190:193], v[46:49]
	v_mfma_i32_16x16x64_i8 v[46:49], v[170:173], v[186:189], v[130:133]
	v_mfma_i32_16x16x64_i8 v[130:133], v[174:177], v[190:193], v[46:49]
	v_mfma_i32_16x16x64_i8 v[46:49], v[162:165], v[194:197], v[118:121]
	v_mfma_i32_16x16x64_i8 v[118:121], v[166:169], v[198:201], v[46:49]
	v_mfma_i32_16x16x64_i8 v[46:49], v[170:173], v[194:197], v[114:117]
	v_mfma_i32_16x16x64_i8 v[114:117], v[174:177], v[198:201], v[46:49]
	v_mfma_i32_16x16x64_i8 v[46:49], v[162:165], v[202:205], v[102:105]
	v_mfma_i32_16x16x64_i8 v[102:105], v[166:169], v[206:209], v[46:49]
	v_mfma_i32_16x16x64_i8 v[46:49], v[170:173], v[202:205], v[98:101]
	v_mfma_i32_16x16x64_i8 v[98:101], v[174:177], v[206:209], v[46:49]
	v_mfma_i32_16x16x64_i8 v[46:49], v[162:165], v[210:213], v[86:89]
	v_mfma_i32_16x16x64_i8 v[86:89], v[166:169], v[214:217], v[46:49]
	v_mfma_i32_16x16x64_i8 v[46:49], v[170:173], v[210:213], v[82:85]
	v_mfma_i32_16x16x64_i8 v[82:85], v[174:177], v[214:217], v[46:49]
	s_setprio 0
	s_barrier
	s_nop 4
	ds_read_b128 v[46:49], v185 offset:49152
	ds_read_b128 v[54:57], v185 offset:50176
	ds_read_b128 v[58:61], v185 offset:51200
	ds_read_b128 v[66:69], v185 offset:52224
	ds_read_b128 v[186:189], v185 offset:53248
	ds_read_b128 v[190:193], v185 offset:54272
	ds_read_b128 v[194:197], v185 offset:55296
	ds_read_b128 v[198:201], v185 offset:56320
	s_add_i32 s62, s82, 0x18000
	s_mov_b32 m0, s62
	s_nop 0
	global_load_lds_dwordx4 v182, s[60:61]
	s_add_i32 s62, s82, 0x1a000
	s_mov_b32 m0, s62
	s_nop 0
	global_load_lds_dwordx4 v183, s[60:61]
	s_add_u32 s50, s50, 0x2080
	s_addc_u32 s51, s51, 0
	s_add_i32 s60, s82, 0x1c000
	s_mov_b32 m0, s60
	s_nop 0
	global_load_lds_dwordx4 v182, s[50:51]
	s_add_i32 s60, s82, 0x1e000
	s_mov_b32 m0, s60
	s_nop 0
	global_load_lds_dwordx4 v183, s[50:51]
	s_waitcnt vmcnt(6)
	s_waitcnt lgkmcnt(0)
	s_barrier
	s_setprio 1
	s_waitcnt lgkmcnt(7)
	v_mfma_i32_16x16x64_i8 v[78:81], v[146:149], v[46:49], v[78:81]
	v_mfma_i32_16x16x64_i8 v[74:77], v[154:157], v[46:49], v[74:77]
	s_waitcnt lgkmcnt(5)
	v_mfma_i32_16x16x64_i8 v[50:53], v[146:149], v[58:61], v[50:53]
	v_mfma_i32_16x16x64_i8 v[42:45], v[154:157], v[58:61], v[42:45]
	s_waitcnt lgkmcnt(3)
	v_mfma_i32_16x16x64_i8 v[30:33], v[146:149], v[186:189], v[30:33]
	v_mfma_i32_16x16x64_i8 v[26:29], v[154:157], v[186:189], v[26:29]
	s_waitcnt lgkmcnt(1)
	v_mfma_i32_16x16x64_i8 v[14:17], v[146:149], v[194:197], v[14:17]
	v_mfma_i32_16x16x64_i8 v[10:13], v[154:157], v[194:197], v[10:13]
	v_mfma_i32_16x16x64_i8 v[78:81], v[150:153], v[54:57], v[78:81]
	v_mfma_i32_16x16x64_i8 v[74:77], v[158:161], v[54:57], v[74:77]
	v_mfma_i32_16x16x64_i8 v[50:53], v[150:153], v[66:69], v[50:53]
	v_mfma_i32_16x16x64_i8 v[42:45], v[158:161], v[66:69], v[42:45]
	v_mfma_i32_16x16x64_i8 v[30:33], v[150:153], v[190:193], v[30:33]
	v_mfma_i32_16x16x64_i8 v[26:29], v[158:161], v[190:193], v[26:29]
	s_waitcnt lgkmcnt(0)
	v_mfma_i32_16x16x64_i8 v[14:17], v[150:153], v[198:201], v[14:17]
	v_mfma_i32_16x16x64_i8 v[10:13], v[158:161], v[198:201], v[10:13]
	v_mfma_i32_16x16x64_i8 v[70:73], v[162:165], v[46:49], v[70:73]
	v_mfma_i32_16x16x64_i8 v[46:49], v[170:173], v[46:49], v[62:65]
	v_mfma_i32_16x16x64_i8 v[38:41], v[162:165], v[58:61], v[38:41]
	v_mfma_i32_16x16x64_i8 v[34:37], v[170:173], v[58:61], v[34:37]
	v_mfma_i32_16x16x64_i8 v[22:25], v[162:165], v[186:189], v[22:25]
	v_mfma_i32_16x16x64_i8 v[18:21], v[170:173], v[186:189], v[18:21]
	v_mfma_i32_16x16x64_i8 v[6:9], v[162:165], v[194:197], v[6:9]
	v_mfma_i32_16x16x64_i8 v[2:5], v[170:173], v[194:197], v[2:5]
	v_mfma_i32_16x16x64_i8 v[70:73], v[166:169], v[54:57], v[70:73]
	v_mfma_i32_16x16x64_i8 v[62:65], v[174:177], v[54:57], v[46:49]
	v_mfma_i32_16x16x64_i8 v[38:41], v[166:169], v[66:69], v[38:41]
	v_mfma_i32_16x16x64_i8 v[34:37], v[174:177], v[66:69], v[34:37]
	v_mfma_i32_16x16x64_i8 v[22:25], v[166:169], v[190:193], v[22:25]
	v_mfma_i32_16x16x64_i8 v[18:21], v[174:177], v[190:193], v[18:21]
	v_mfma_i32_16x16x64_i8 v[6:9], v[166:169], v[198:201], v[6:9]
	v_mfma_i32_16x16x64_i8 v[2:5], v[174:177], v[198:201], v[2:5]
	s_setprio 0
	s_barrier
	s_add_i32 s79, s79, 2
	s_add_u32 s76, s76, 0x100
	s_addc_u32 s77, s77, 0
	s_add_u32 s2, s2, 0x100
	s_addc_u32 s3, s3, 0
	s_cmp_gt_u32 s79, 5
	s_branch .LBB0_214

; #define PG8_BAR __builtin_amdgcn_s_barrier()
; #define PROF_BEGIN(sel) do { if constexpr (PROF && PROF_SEL == (sel)) prof_t0 = (unsigned)__builtin_amdgcn_s_memrealtime(); } while (0)
; #define PROF_END(sel) do { if constexpr (PROF && PROF_SEL == (sel)) prof_acc += (unsigned)__builtin_amdgcn_s_memrealtime() - prof_t0; } while (0)
;     __device__ __forceinline__ bool next(int i, pg8::Unit& u) const { const int L = i * G + c; if (L >= nM * 4) return false; int pm, pn; pg8::tile_remap<4>(L, nM, pm, pn); if (rev) pm = nM - 1 - pm; u.pm = pm; u.pn = pn; u.aux = 0; u.skip = 0; return true; }
;     __device__ __forceinline__ bool next(int i, pg8::Unit& u) const { const int L = first + i * stride; if (i >= nmine || L >= 512) return false; u.pm = L & 3; u.pn = (L >> 2) & 3; u.aux = L >> 4; u.skip = 0; return true; }
;     __device__ __forceinline__ bool next(int i, pg8::Unit& u) const { if (!TW) { const bool r = Base::next(i, u); u.skip = 0; return r; } const bool r = Base::next(i >> 1, u); u.skip = !(i & 1); return r; }
; template <class Epi, class Sched, bool F8 = false, bool PF = false, bool I8 = false, int PID = -1>
; __device__ __forceinline__ void gemm_phase(LAS unsigned char* lds, LAS unsigned char* xlds, const int RP, const int RPB, const int nt, const Sched& S, const Epi& E, const int stagger_ticks) {
;     ...
;         PROF_END(1); PROF_BEGIN(3);
;         if (wr == 0) PG8_BAR;
;         Unit nn; bool has_nn = false; unsigned gv[4] = {vA0, vA1, vA2, vA3};
;         if (has_next) { has_nn = S.next(ui + 2, nn); if (Sched::GATHER) { if (has_nn) S.a_offsets(nn, Rr, Cc, RP, gv); } }
.LBB0_218:
	s_add_u32 s100, s10, 0x80
	s_addc_u32 s101, s11, 0
	s_add_i32 s98, s7, 0x8000
	s_mov_b32 m0, s98
	s_nop 0
	global_load_lds_dwordx4 v180, s[100:101]
	s_add_i32 s98, s7, 0xa000
	s_mov_b32 m0, s98
	s_nop 0
	global_load_lds_dwordx4 v181, s[100:101]
	s_add_u32 s100, s100, 0x20000
	s_addc_u32 s101, s101, 0
	s_add_i32 s98, s7, 0xc000
	s_mov_b32 m0, s98
	s_nop 0
	global_load_lds_dwordx4 v180, s[100:101]
	s_add_i32 s98, s7, 0xe000
	s_mov_b32 m0, s98
	s_nop 0
	global_load_lds_dwordx4 v181, s[100:101]
	v_cndmask_b32_e64 v46, 0, 1, s[20:21]
	v_cmp_ne_u32_e64 s[0:1], 1, v46
	s_andn2_b64 vcc, exec, s[20:21]
	s_cbranch_vccnz .LBB0_225
	s_add_i32 s2, s9, 2
	s_mul_i32 s46, s2, s92
	s_add_i32 s46, s46, s33
	s_cmpk_gt_i32 s46, 0xaff
	s_mov_b64 s[20:21], 0
	s_cbranch_scc1 .LBB0_226
	s_cmpk_gt_i32 s46, 0x9ff
	s_mov_b64 s[2:3], -1
	s_cbranch_scc0 .LBB0_222
	s_add_i32 s2, s46, 0xfffff600
	s_lshr_b32 s22, s2, 3
	s_and_b32 s18, s46, 7
	s_mov_b64 s[2:3], 0
